# grid barrier seams k1-k9: shared lane-0 routine, globally last arriver releases all XCD generation words directly, episode counter instead of divisions
# speedup vs baseline: 1.0135x; 1.0048x over previous
; #define LAS __attribute__((address_space(3)))
; __device__ __forceinline__ unsigned xb_add(unsigned* p, unsigned v) { return __hip_atomic_fetch_add(p, v, __ATOMIC_RELAXED, __HIP_MEMORY_SCOPE_AGENT); }
; __device__ __forceinline__ unsigned xb_xcc_id() { return (unsigned)__builtin_amdgcn_s_getreg((3 << 11) | 20) & 0xFu; }
; __device__ __forceinline__ XcdBarrier xcd_barrier_post(unsigned* bar, volatile LAS unsigned* st) {
;     XcdBarrier b; b.bar = bar; b.x = xb_xcc_id(); b.st = st;
;     if (threadIdx.x == 0) (void)xb_add(&bar[XB_XCNT(b.x)], 1u);
;     return b;
; }
; __global__ void __launch_bounds__(NWAVES * 64, 2) fwd(Params P) {
;     ...
;     volatile LAS unsigned* MISC = (volatile LAS unsigned*)(lds + MISC_OFF);
;     const int tid0 = threadIdx.x;
;     const int G0 = gridDim.x, bx0 = blockIdx.x;
;     const int vcu0 = (G0 % 8 == 0) ? (bx0 % 8) * (G0 / 8) + bx0 / 8 : bx0;
;     unsigned* ctl = (unsigned*)(P.ws + WS_CTL);
;     if (tid0 < 64) MISC[tid0] = 0u;
;     __syncthreads();
;     ...
;     constexpr int lo = 0, hi = 64;
;     ...
;     const int lo = P.ph_lo, hi = P.ph_hi;
;     ...
;     XcdBarrier bar; bar.bar = ctl + CW_BAR + P.bar_idx * XCD_BAR_WORDS; bar.x = 0; bar.st = MISC + 8;
;     if (hi - lo > 1) bar = xcd_barrier_post(ctl + CW_BAR + P.bar_idx * XCD_BAR_WORDS, MISC + 8);
.LBB0_2:
	s_load_dwordx2 s[0:1], s[74:75], 0x120
	v_cmp_gt_u32_e32 vcc, 64, v0
	s_waitcnt lgkmcnt(0)
	v_writelane_b32 v253, s0, 4
	s_nop 1
	v_writelane_b32 v253, s1, 5
	s_and_saveexec_b64 s[0:1], vcc
	v_lshl_add_u32 v1, v0, 2, 0
	v_add_u32_e32 v1, 0x23f00, v1
	v_mov_b32_e32 v2, 0
	ds_write_b32 v1, v2
	s_or_b64 exec, exec, s[0:1]
	s_waitcnt lgkmcnt(0)
	s_barrier
	s_mov_b32 s101, 0
	s_load_dword s0, s[74:75], 0x130
	s_load_dwordx2 s[4:5], s[74:75], 0x120
	s_getreg_b32 s2, hwreg(HW_REG_XCC_ID, 0, 4)
	s_mov_b32 s93, 0
	s_waitcnt lgkmcnt(0)
	s_mulk_i32 s0, 0xd80
	s_ashr_i32 s1, s0, 31
	s_lshl_b64 s[0:1], s[0:1], 2
	s_add_u32 s0, s4, s0
	s_addc_u32 s1, s5, s1
	s_add_u32 s44, s0, 0x4000
	s_addc_u32 s45, s1, 0
	s_and_b32 s0, s2, 15
	v_writelane_b32 v253, s0, 6
	s_lshl_b32 s4, s0, 6
	v_cmp_eq_u32_e64 s[2:3], 0, v0
	s_mov_b64 s[0:1], exec
	s_nop 0
	v_writelane_b32 v253, s2, 7
	s_nop 1
	v_writelane_b32 v253, s3, 8
	s_and_b64 s[2:3], s[0:1], s[2:3]
	s_mov_b64 exec, s[2:3]
	s_cbranch_execz .LBB0_7
	s_mov_b64 s[2:3], exec
	v_mbcnt_lo_u32_b32 v1, s2, 0
	v_mbcnt_hi_u32_b32 v1, s3, v1
	v_cmp_eq_u32_e32 vcc, 0, v1
	s_and_b64 s[6:7], exec, vcc
	s_mov_b64 exec, s[6:7]
	s_cbranch_execz .LBB0_7
	s_lshl_b32 s5, s4, 2
	s_bcnt1_i32_b64 s2, s[2:3]
	v_mov_b32_e32 v1, s5
	v_mov_b32_e32 v2, s2
	global_atomic_add v1, v2, s[44:45] offset:1024

; __device__ __forceinline__ void xcd_barrier(const XcdBarrier& b) {
;     ...
;     __syncthreads();
; __global__ void __launch_bounds__(NWAVES * 64, 2) fwd(Params P) {
;     ...
;     for (int l = 0; l < 4; ++l) {
.LBB0_9:
	s_or_b64 exec, exec, s[2:3]
	s_add_i32 s101, s101, 1
	s_add_u32 s14, s14, 1
	s_addc_u32 s15, s15, 0
	s_cmp_eq_u32 s14, 4
	s_waitcnt lgkmcnt(0)
	s_barrier
	s_cbranch_scc0 .LBB0_10
	s_getpc_b64 s[98:99]

; #define SEAM(k) do { if (((k) & 15) == 3 && TS_ON(21)) { TS_END(21); } if ((k) + 1 < hi) { TS_END((k) & 15); TS_BEGIN(20); xcd_barrier(bar); if ((MK_DBL >> 19) & 1) xcd_barrier(bar); TS_END(20); } else { TS_END((k) & 15); } } while (0)
; __device__ __forceinline__ void xcd_barrier(const XcdBarrier& b) {
;     ...
;     __syncthreads();
; __global__ void __launch_bounds__(NWAVES * 64, 2) fwd(Params P) {
;     ...
;             SEAM(pb + 0);
.LBB0_237:
	s_or_b64 exec, exec, s[2:3]
	s_add_i32 s101, s101, 1
	s_waitcnt lgkmcnt(0)
	s_barrier

; #define LAS __attribute__((address_space(3)))
; __device__ __forceinline__ void xcd_barrier(const XcdBarrier& b) {
;     asm volatile("s_waitcnt vmcnt(0)" ::: "memory");
;     __syncthreads();
;     if (threadIdx.x == 0) {
;         unsigned* bar = b.bar;
;         __builtin_amdgcn_s_waitcnt(0);
;         unsigned nloc = b.st[0], nx = b.st[1];
;         if (nloc == 0u) { xcd_barrier_complete(bar, b.x, nloc, nx); b.st[0] = nloc; b.st[1] = nx; }
;         const unsigned old = xb_add(&bar[XB_XSUB(b.x)], 1u);
;         const unsigned gen = old / nloc;
;         if (old + 1u == (gen + 1u) * nloc) {
;             __builtin_amdgcn_fence(__ATOMIC_RELEASE, "agent");
;             asm volatile("s_waitcnt vmcnt(0)" ::: "memory");
;             const unsigned og = xb_add(&bar[XB_TOP], 1u);
;             const unsigned tg = og / nx;
;             if (og + 1u == (tg + 1u) * nx) xb_add(&bar[XB_TOPGEN], 1u);
;             else XB_SPIN(xb_ld(&bar[XB_TOPGEN]) == tg, bar);
;             __builtin_amdgcn_fence(__ATOMIC_ACQUIRE, "agent");
;             xb_add(&bar[XB_XGEN(b.x)], 1u);
;             asm volatile("s_waitcnt vmcnt(0)" ::: "memory");
;         } else {
;             XB_SPIN(xb_ld(&bar[XB_XGEN(b.x)]) == gen, bar);
;             __builtin_amdgcn_fence(__ATOMIC_ACQUIRE, "agent");
;             asm volatile("s_waitcnt vmcnt(0)" ::: "memory");
;         }
;     }
;     __syncthreads();
; __device__ __forceinline__ void lora_phase(LAS unsigned char* lds, const bf16_t* projb, const float* mix, const float* vmix, const bf16_t* Wl_w, const bf16_t* Wl_a, const bf16_t* Wl_g, const bf16_t* Wl_v, ...
;     const int wave = __builtin_amdgcn_readfirstlane(tid >> 6), lane = tid & 63, fr = lane & 15, fq = lane >> 4;
;     LAS bf16_t* Aimg = (LAS bf16_t*)lds;
;     for (int u = vcu; u < M / 64; u += G) {
;         {
;             const int tau = tid >> 3, part = tid & 7, m = u * 64 + tau; const bool first = (m % SEQ) == 0;
; #pragma unroll
;             for (int i = 0; i < 5; ++i) {
;                 const int j0 = 40 * part + 8 * i;
;                 const u32x4 cur = *(const u32x4*)(projb + (size_t)m * PROJ_BLD + OFF_WLO + j0);
;                 u32x4 prv = (u32x4){0u, 0u, 0u, 0u};
;                 if (!first) prv = *(const u32x4*)(projb + (size_t)(m - 1) * PROJ_BLD + OFF_WLO + j0);
;                 f32x4 mx0, mx1;
.LBB0_254:
	s_waitcnt vmcnt(0)
	s_waitcnt vmcnt(0)
	s_barrier
	s_mov_b64 s[2:3], exec
	v_readlane_b32 s4, v253, 7
	v_readlane_b32 s5, v253, 8
	s_and_b64 s[4:5], s[2:3], s[4:5]
	s_mov_b64 exec, s[4:5]
	s_cbranch_execz .LBB0_306
	s_mov_b32 s100, 1
	s_branch .Lxb_common
.Lxb_ret_1:
.LBB0_306:
	s_or_b64 exec, exec, s[2:3]
	s_add_i32 s101, s101, 1
	s_mov_b32 s38, s93
	s_waitcnt lgkmcnt(0)
	s_barrier
	s_ashr_i32 s39, s38, 31
	v_readlane_b32 s2, v253, 4
	v_readlane_b32 s3, v253, 5
	s_add_u32 s36, s2, s38
	v_readlane_b32 s2, v253, 2
	s_addc_u32 s37, s3, s39
	s_add_i32 s60, s38, s2
	v_readlane_b32 s2, v253, 3
	s_add_i32 s61, s38, s2
	s_add_u32 s24, s36, 0x16400000
	s_addc_u32 s25, s37, 0
	s_lshl_b64 s[2:3], s[38:39], 3
	v_readlane_b32 s4, v254, 3
	v_readlane_b32 s5, v254, 4
	s_add_u32 s42, s4, s2
	v_mov_b32_e32 v137, v0
	s_addc_u32 s43, s5, s3
	s_load_dwordx2 s[30:31], s[42:43], 0x48
	s_add_u32 s28, s36, 0x22400000
	s_addc_u32 s29, s37, 0
	v_sub_u32_e64 v1, s14, 1 clamp
	s_cmpk_lt_i32 s61, 0x100
	s_mul_hi_u32 s41, s14, 0xd20
	s_mul_i32 s40, s14, 0xd20
	v_readfirstlane_b32 s39, v1
	v_readfirstlane_b32 s4, v137
	s_cselect_b64 s[2:3], -1, 0
	s_cmpk_gt_i32 s61, 0xff
	v_and_b32_e32 v136, 15, v137
	s_cbranch_scc1 .LBB0_378
	s_load_dwordx2 s[6:7], s[42:43], 0x50
	s_cmp_lg_u32 s14, 0
	s_cselect_b64 s[44:45], -1, 0
	s_lshl_b32 s92, s39, 5
	s_lshl_b64 s[8:9], s[92:93], 2
	s_waitcnt lgkmcnt(0)
	s_add_u32 s10, s6, s8
	s_addc_u32 s11, s7, s9
	s_lshl_b64 s[6:7], s[40:41], 2
	s_add_u32 s6, s30, s6
	v_and_b32_e32 v11, 7, v137
	s_addc_u32 s7, s31, s7
	v_mul_u32_u24_e32 v138, 40, v11
	s_lshl_b32 s4, s4, 1
	s_and_b32 s20, s4, 0xffffff80
	v_lshlrev_b32_e32 v6, 2, v138
	v_mov_b32_e32 v7, v3
	v_ashrrev_i32_e32 v1, 3, v137
	s_movk_i32 s5, 0x290
	s_ashr_i32 s21, s20, 31
	v_lshl_add_u64 v[8:9], s[6:7], 0, v[6:7]
	v_lshl_add_u64 v[144:145], s[10:11], 0, v[6:7]
	v_mov_b32_e32 v7, 0xffffff90
	v_mul_lo_u32 v2, v1, s5
	s_lshl_b64 s[4:5], s[20:21], 1
	v_mad_u32_u24 v7, v11, 40, v7
	v_lshlrev_b32_e32 v4, 1, v136
	s_add_u32 s4, s28, s4
	v_cmp_gt_u32_e64 s[12:13], s50, v7
	v_mov_b32_e32 v7, 0xffffff98
	v_and_b32_e32 v12, 24, v4
	v_and_b32_e32 v4, 48, v137
	s_addc_u32 s5, s29, s5
	v_mov_b32_e32 v5, v3
	v_mad_u32_u24 v7, v11, 40, v7
	v_lshl_add_u64 v[140:141], s[4:5], 0, v[4:5]
	s_mov_b64 s[4:5], 0x3000
	v_mov_b32_e32 v6, 0xffffff88
	v_cmp_gt_u32_e64 s[16:17], s50, v7
	v_mov_b32_e32 v7, 0xffffffa0
	v_and_b32_e32 v13, 3, v137
	v_lshl_add_u64 v[142:143], v[8:9], 0, s[4:5]
	v_lshlrev_b32_e32 v8, 1, v138
	v_mad_u32_u24 v6, v11, 40, v6
	v_mad_u32_u24 v7, v11, 40, v7
	v_add3_u32 v139, 0, v2, v8
	v_mad_u32_u24 v2, v11, 40, 8
	v_cmp_gt_u32_e64 s[10:11], s50, v6
	v_mad_u32_u24 v6, v11, 40, 16
	v_mad_u32_u24 v8, v11, 40, 24
	v_mad_u32_u24 v10, v11, 40, 32
	v_cmp_gt_u32_e64 s[18:19], s50, v7
	v_or3_b32 v146, v12, v13, s20
	v_mul_u32_u24_e32 v7, 0x290, v136
	v_cmp_lt_u32_e64 s[4:5], 1, v11
	v_cmp_lt_u32_e64 s[6:7], 3, v11
	v_cmp_ne_u32_e64 s[8:9], 7, v11
	v_cmp_ne_u32_e64 s[14:15], 0, v11
	v_or_b32_e32 v148, 4, v146
	v_or_b32_e32 v150, 32, v146
	v_or_b32_e32 v152, 36, v146
	v_or_b32_e32 v154, 64, v146
	v_or_b32_e32 v156, 0x44, v146
	v_or_b32_e32 v158, 0x60, v146
	v_or_b32_e32 v160, 0x64, v146
	v_lshl_add_u64 v[162:163], s[36:37], 0, v[4:5]
	v_add3_u32 v147, 0, v4, v7
	v_lshlrev_b32_e32 v164, 1, v2
	v_lshlrev_b32_e32 v166, 1, v6
	v_lshlrev_b32_e32 v168, 1, v8
	v_lshlrev_b32_e32 v170, 1, v10
	s_mov_b32 s50, s61

; __device__ __forceinline__ unsigned xb_ld(unsigned* p)              { return __hip_atomic_load(p, __ATOMIC_RELAXED, __HIP_MEMORY_SCOPE_AGENT); }
; __device__ __forceinline__ unsigned xb_add(unsigned* p, unsigned v) { return __hip_atomic_fetch_add(p, v, __ATOMIC_RELAXED, __HIP_MEMORY_SCOPE_AGENT); }
; #define XB_SPIN(cond, bar) do { unsigned _sp = 0; while (cond) { __builtin_amdgcn_s_sleep(1); \
;     if ((++_sp & 255u) == 0u) { if (xb_ld(&(bar)[XB_TMO])) break; if (_sp > XB_SPIN_CAP) { atomicAdd(&(bar)[XB_TMO], 1u); break; } } } } while (0)
; __device__ __forceinline__ void xcd_barrier(const XcdBarrier& b) {
;     asm volatile("s_waitcnt vmcnt(0)" ::: "memory");
;     __syncthreads();
;     if (threadIdx.x == 0) {
;         unsigned* bar = b.bar;
;         __builtin_amdgcn_s_waitcnt(0);
;         unsigned nloc = b.st[0], nx = b.st[1];
;         if (nloc == 0u) { xcd_barrier_complete(bar, b.x, nloc, nx); b.st[0] = nloc; b.st[1] = nx; }
;         const unsigned old = xb_add(&bar[XB_XSUB(b.x)], 1u);
;         const unsigned gen = old / nloc;
;         if (old + 1u == (gen + 1u) * nloc) {
;             __builtin_amdgcn_fence(__ATOMIC_RELEASE, "agent");
;             asm volatile("s_waitcnt vmcnt(0)" ::: "memory");
;             const unsigned og = xb_add(&bar[XB_TOP], 1u);
;             const unsigned tg = og / nx;
;             if (og + 1u == (tg + 1u) * nx) xb_add(&bar[XB_TOPGEN], 1u);
;             else XB_SPIN(xb_ld(&bar[XB_TOPGEN]) == tg, bar);
;             __builtin_amdgcn_fence(__ATOMIC_ACQUIRE, "agent");
;             xb_add(&bar[XB_XGEN(b.x)], 1u);
;             asm volatile("s_waitcnt vmcnt(0)" ::: "memory");
;         } else {
;             XB_SPIN(xb_ld(&bar[XB_XGEN(b.x)]) == gen, bar);
;             __builtin_amdgcn_fence(__ATOMIC_ACQUIRE, "agent");
;             asm volatile("s_waitcnt vmcnt(0)" ::: "memory");
;         }
;     }
;     __syncthreads();
; __global__ void __launch_bounds__(NWAVES * 64, 2) fwd(Params P) {
;     ...
;         if (IN(pb + 3)) {
;             PH_BEGIN
;             TS_BEGIN(3);
;     ...
;             RW_ARGS(a);
;             const bool ssd_first = ((vcu >> 1) & 1) != 0;
;             if (ssd_first) { int tid4 = tid; asm volatile("" : "+v"(tid4)); ssd_scan_phase(lds, xbcc, dtb, INP(6) + l * SSD_H, INP(7) + l * SSD_H, (bf16_t*)yssd, vcu, G, tid4); }
.LBB0_606:
	s_waitcnt vmcnt(0)
	v_writelane_b32 v254, s40, 18
	s_waitcnt lgkmcnt(0)
	s_barrier
	v_writelane_b32 v254, s41, 19
	s_mov_b64 s[2:3], exec
	v_readlane_b32 s4, v253, 7
	v_readlane_b32 s5, v253, 8
	v_readlane_b32 s24, v253, 63
	v_readlane_b32 s60, v254, 5
	v_readlane_b32 s28, v253, 9
	v_readlane_b32 s34, v253, 11
	v_readlane_b32 s38, v253, 13
	v_readlane_b32 s40, v253, 17
	s_and_b64 s[4:5], s[2:3], s[4:5]
	v_readlane_b32 s25, v254, 0
	v_readlane_b32 s61, v254, 6
	v_readlane_b32 s29, v253, 10
	v_readlane_b32 s35, v253, 12
	v_readlane_b32 s39, v253, 14
	v_readlane_b32 s41, v253, 18
	s_mov_b64 exec, s[4:5]
	s_cbranch_execz .LBB0_658
	s_mov_b32 s100, 2
	s_branch .Lxb_common
.Lxb_ret_2:
.LBB0_658:
	s_or_b64 exec, exec, s[2:3]
	s_add_i32 s101, s101, 1
	s_mov_b32 s4, s93
	s_waitcnt lgkmcnt(0)
	s_barrier
	s_ashr_i32 s5, s4, 31
	v_readlane_b32 s2, v253, 4
	v_readlane_b32 s3, v253, 5
	s_add_u32 s15, s2, s4
	v_readlane_b32 s2, v253, 2
	s_addc_u32 s16, s3, s5
	s_add_i32 s2, s4, s2
	v_writelane_b32 v254, s2, 20
	v_readlane_b32 s2, v253, 3
	s_add_i32 s74, s4, s2
	v_writelane_b32 v254, s4, 21
	s_lshl_b64 s[2:3], s[4:5], 3
	s_waitcnt vmcnt(0)
	v_mov_b32_e32 v1, v0
	v_writelane_b32 v254, s5, 22
	s_nop 0
	v_readlane_b32 s4, v254, 3
	v_readlane_b32 s5, v254, 4
	s_add_u32 s8, s4, s2
	s_addc_u32 s9, s5, s3
	s_add_u32 s2, s8, s64
	s_addc_u32 s3, s9, 0
	s_load_dwordx2 s[2:3], s[2:3], 0x0
	s_add_u32 s4, s8, s63
	s_addc_u32 s5, s9, 0
	s_add_u32 s6, s8, s62
	v_writelane_b32 v254, s8, 23
	s_addc_u32 s7, s9, 0
	s_bitcmp0_b32 s74, 1
	v_writelane_b32 v254, s9, 24
	s_waitcnt lgkmcnt(0)
	v_writelane_b32 v254, s2, 25
	s_cselect_b64 s[78:79], -1, 0
	s_and_b64 vcc, exec, s[78:79]
	v_writelane_b32 v254, s3, 26
	s_load_dwordx2 s[2:3], s[4:5], 0x0
	s_waitcnt lgkmcnt(0)
	v_writelane_b32 v254, s2, 27
	s_nop 1
	v_writelane_b32 v254, s3, 28
	s_load_dwordx2 s[2:3], s[6:7], 0x0
	s_waitcnt lgkmcnt(0)
	v_writelane_b32 v254, s2, 29
	s_nop 1
	v_writelane_b32 v254, s3, 30
	s_cbranch_vccnz .LBB0_733
	v_mov_b32_e32 v2, v1
	s_cmpk_gt_i32 s74, 0xff
	v_readfirstlane_b32 s2, v2
	s_cbranch_scc1 .LBB0_733
	s_add_u32 s4, s15, 0x32400000
	s_addc_u32 s5, s16, 0
	v_writelane_b32 v254, s78, 31
	s_add_u32 s6, s15, 0x35400000
	s_addc_u32 s7, s16, 0
	v_writelane_b32 v254, s79, 32
	v_writelane_b32 v254, s6, 33
	v_and_b32_e32 v7, 63, v2
	v_ashrrev_i32_e32 v106, 2, v2
	v_writelane_b32 v254, s7, 34
	v_and_b32_e32 v10, 3, v2
	v_readlane_b32 s6, v254, 23
	v_readlane_b32 s7, v254, 24
	s_load_dwordx4 s[8:11], s[6:7], 0x30
	v_readlane_b32 s6, v254, 9
	v_readlane_b32 s7, v254, 10
	s_lshl_b64 s[6:7], s[6:7], 2
	v_lshlrev_b32_e32 v7, 3, v7
	s_waitcnt lgkmcnt(0)
; #define LAS __attribute__((address_space(3)))
; __device__ __forceinline__ void ssd_scan_phase(LAS unsigned char* lds, const bf16_t* xbcc, const float* dtb, const float* a_log, const float* dskip, bf16_t* yssd, const int vcu, const int G, const int tid) {
;     const int wave = __builtin_amdgcn_readfirstlane(tid >> 6), lane = tid & 63, fr = lane & 15, fq = lane >> 4;
;     const int lt = (wave < 4) ? 2 * wave : 15 - 2 * wave;
;     LAS bf16_t* Cimg = (LAS bf16_t*)(lds + SS_C); LAS bf16_t* Bimg = (LAS bf16_t*)(lds + SS_B); LAS bf16_t* BTimg = (LAS bf16_t*)(lds + SS_BT);
;     LAS bf16_t* xT = (LAS bf16_t*)(lds + SS_XT); LAS bf16_t* xwT = (LAS bf16_t*)(lds + SS_XW); LAS bf16_t* hT = (LAS bf16_t*)(lds + SS_HT);
;     LAS float* acum = (LAS float*)(lds + SS_AC); LAS float* dtv = (LAS float*)(lds + SS_DT);
;     for (int u = vcu; u < BATCH * SSD_H * 2; u += G) {
;         const int b = u >> 5, h = (u >> 1) & 15, phalf = u & 1, g = h >> 3;
;         const float Ah = -expf(a_log[h]) * 1.4426950408889634f;
;         const float dsk = dskip[h];
;         f32x4 hs[2] = {(f32x4){0.f, 0.f, 0.f, 0.f}, (f32x4){0.f, 0.f, 0.f, 0.f}};
;         for (int i = tid; i < 32 * SP / 2; i += 512) ((LAS unsigned*)hT)[i] = 0u;
;         const int row = tid >> 2, part = tid & 3;
;         u32x4 cvn[4], bvn[4], xrn; float dtn = 0.f, dtn1 = 0.f;
	s_add_u32 s8, s8, s6
	s_addc_u32 s9, s9, s7
	v_writelane_b32 v254, s8, 35
	s_add_u32 s6, s10, s6
	s_addc_u32 s7, s11, s7
	v_writelane_b32 v254, s9, 36
	v_writelane_b32 v254, s6, 37
	s_add_u32 s3, s15, 0x35500000
	v_readlane_b32 s11, v253, 52
	v_writelane_b32 v254, s7, 38
	v_writelane_b32 v254, s15, 39
	v_writelane_b32 v254, s3, 40
	v_writelane_b32 v254, s16, 41
	s_addc_u32 s3, s16, 0
	s_ashr_i32 s8, s2, 6
	v_writelane_b32 v254, s3, 42
	s_lshl_b32 s3, s8, 1
	s_sub_i32 s6, 15, s3
	s_cmp_lt_i32 s8, 4
	s_cselect_b32 s24, s3, s6
	s_movk_i32 s3, 0x880
	s_cmp_lt_u32 s2, 64
	v_cmp_gt_i32_e64 s[6:7], s3, v2
	s_cselect_b64 s[2:3], -1, 0
	s_add_i32 s9, 0, 0x20000
	s_movk_i32 s10, 0x110
	v_add_u32_e32 v108, s9, v7
	v_add_u32_e32 v109, s11, v7
	v_mul_lo_u32 v7, v106, s10
	v_lshlrev_b32_e32 v8, 6, v10
	v_and_b32_e32 v5, 15, v2
	v_add3_u32 v110, 0, v7, v8
	v_and_b32_e32 v7, -4, v2
	v_and_b32_e32 v115, 48, v2
	v_bfe_u32 v9, v2, 4, 2
	v_add_u32_e32 v111, s9, v7
	v_add_u32_e32 v118, s9, v115
	v_readlane_b32 s28, v253, 53
	v_lshl_or_b32 v15, s8, 4, v5
	s_add_i32 s9, 0, 0x11000
	s_lshl_b32 s8, s8, 5
	v_mul_u32_u24_e32 v17, 0x2200, v10
	v_lshlrev_b32_e32 v18, 1, v106
	v_add_u32_e32 v112, s11, v7
	v_add_u32_e32 v7, 0x88, v106
	v_lshl_or_b32 v113, s24, 4, v5
	v_lshlrev_b32_e32 v119, 3, v9
	s_add_i32 s8, s28, s8
	v_add3_u32 v122, s9, v17, v18
	v_mul_u32_u24_e32 v17, 0x440, v10
	v_mul_lo_u32 v8, v113, s10
	v_lshl_add_u32 v116, v113, 2, s11
	v_add_u32_e32 v117, s11, v115
	v_readlane_b32 s11, v253, 54
	v_mul_lo_u32 v15, v15, s10
	v_readlane_b32 s10, v253, 55
	v_add_u32_e32 v16, s8, v119
	v_add_lshl_u32 v18, v17, v106, 1
	v_add_lshl_u32 v17, v7, v17, 1
	s_movk_i32 s8, 0x440
	v_writelane_b32 v254, s6, 44
	v_add_u32_e32 v114, 0, v8
	v_lshlrev_b32_e32 v8, 2, v9
	v_add_u32_e32 v124, s11, v17
	v_add_u32_e32 v126, s10, v17
	v_mad_u32_u24 v17, v10, s8, v237
	v_writelane_b32 v254, s7, 45
	v_add_u32_e32 v123, s11, v18
	v_add_u32_e32 v125, s10, v18
	v_add_lshl_u32 v18, v17, v106, 1
	v_add_lshl_u32 v17, v17, v7, 1
	v_cmp_gt_i32_e64 s[30:31], v8, v113
	v_lshlrev_b32_e32 v4, 5, v10
	v_lshlrev_b32_e32 v6, 3, v10
	v_add_u32_e32 v128, s11, v17
	v_add_u32_e32 v130, s10, v17
	v_mad_u32_u24 v17, v10, s8, v238
	v_mad_u32_u24 v10, v10, s8, v239
	v_writelane_b32 v254, s30, 46
	v_add_u32_e32 v127, s11, v18
	v_add_u32_e32 v129, s10, v18
	v_add_lshl_u32 v18, v17, v106, 1
	v_add_lshl_u32 v17, v17, v7, 1
	v_add_lshl_u32 v7, v10, v7, 1
	v_writelane_b32 v254, s31, 47
	v_cmp_lt_i32_e64 s[30:31], v8, v113
	v_add_u32_e32 v136, s11, v7
	v_add_u32_e32 v138, s10, v7
	v_writelane_b32 v254, s30, 48
	v_or_b32_e32 v7, 3, v8
	v_add_u32_e32 v132, s11, v17
	v_writelane_b32 v254, s31, 49
	v_cmp_gt_i32_e64 s[30:31], v7, v113
	v_add_u32_e32 v134, s10, v17
	v_add_lshl_u32 v17, v10, v106, 1
	v_or_b32_e32 v10, 2, v8
	v_writelane_b32 v254, s30, 50
	v_or_b32_e32 v7, 17, v8
	s_cmp_gt_i32 s24, -1
	v_writelane_b32 v254, s31, 51
	v_cmp_gt_i32_e64 s[30:31], v10, v113
	v_or_b32_e32 v10, 16, v8
	v_add3_u32 v121, s9, v15, v115
	v_writelane_b32 v254, s30, 52
	s_cselect_b64 s[8:9], -1, 0
	s_cmp_gt_i32 s24, 0
	v_writelane_b32 v254, s31, 53
	v_cmp_gt_i32_e64 s[30:31], v7, v113
	v_or_b32_e32 v7, 19, v8
	v_add_u32_e32 v13, s11, v115
	v_writelane_b32 v254, s30, 54
	v_lshl_add_u32 v14, v113, 1, s11
	v_add_u32_e32 v15, s10, v115
	v_writelane_b32 v254, s31, 55
	v_cmp_gt_i32_e64 s[30:31], v10, v113
	v_or_b32_e32 v10, 18, v8
	v_add_u32_e32 v131, s11, v18
	v_writelane_b32 v254, s30, 56
	v_add_u32_e32 v133, s10, v18
	v_add_u32_e32 v135, s11, v17
	v_writelane_b32 v254, s31, 57
	v_cmp_gt_i32_e64 s[30:31], v7, v113
	v_or_b32_e32 v7, 33, v8
	v_add_u32_e32 v137, s10, v17
	v_writelane_b32 v254, s30, 58
	s_cselect_b64 s[10:11], -1, 0
	s_cmp_gt_i32 s24, 1
	v_writelane_b32 v254, s31, 59
	v_cmp_gt_i32_e64 s[30:31], v10, v113
	v_or_b32_e32 v10, 32, v8
	s_cselect_b64 s[12:13], -1, 0
	v_writelane_b32 v254, s30, 60
	s_cmp_gt_i32 s24, 2
	s_cselect_b64 s[14:15], -1, 0
	v_writelane_b32 v254, s31, 61
	v_cmp_gt_i32_e64 s[30:31], v7, v113
	v_or_b32_e32 v7, 35, v8
	s_cmp_gt_i32 s24, 3
	v_writelane_b32 v254, s30, 62
	s_cselect_b64 s[16:17], -1, 0
	s_cmp_gt_i32 s24, 4
	v_writelane_b32 v254, s31, 63
	v_cmp_gt_i32_e64 s[30:31], v10, v113
	v_or_b32_e32 v10, 34, v8
	s_cselect_b64 s[18:19], -1, 0
	v_writelane_b32 v255, s30, 0
	s_cmp_gt_i32 s24, 5
	s_cselect_b64 s[20:21], -1, 0
	v_writelane_b32 v255, s31, 1
	v_cmp_gt_i32_e64 s[30:31], v7, v113
	v_or_b32_e32 v7, 49, v8
	s_cmp_gt_i32 s24, 6
	v_writelane_b32 v255, s30, 2
	v_add_u32_e32 v12, s28, v115
	s_cselect_b64 s[22:23], -1, 0
	v_writelane_b32 v255, s31, 3
	v_cmp_gt_i32_e64 s[30:31], v10, v113
	v_or_b32_e32 v10, 48, v8
	s_cmp_gt_i32 s24, -2
	v_writelane_b32 v255, s30, 4
	v_lshl_add_u32 v140, v2, 2, s28
	v_readlane_b32 s28, v254, 20
	v_writelane_b32 v255, s31, 5
	v_cmp_gt_i32_e64 s[30:31], v7, v113
	v_or_b32_e32 v7, 51, v8
	v_cmp_gt_i32_e64 s[38:39], v7, v113
	v_writelane_b32 v255, s30, 6
	v_or_b32_e32 v7, 0x41, v8
	v_cmp_gt_i32_e64 s[42:43], v7, v113
	v_writelane_b32 v255, s31, 7
	v_cmp_gt_i32_e64 s[30:31], v10, v113
	v_or_b32_e32 v10, 50, v8
	v_cmp_gt_i32_e64 s[40:41], v10, v113
	v_or_b32_e32 v10, 64, v8
	v_or_b32_e32 v7, 0x43, v8
	v_cmp_gt_i32_e64 s[44:45], v10, v113
	v_or_b32_e32 v10, 0x42, v8
	v_cmp_gt_i32_e64 s[46:47], v7, v113
	v_or_b32_e32 v7, 0x51, v8
	v_cmp_gt_i32_e64 s[48:49], v10, v113
	v_or_b32_e32 v10, 0x50, v8
	v_cmp_gt_i32_e64 s[50:51], v7, v113
	v_or_b32_e32 v7, 0x53, v8
	v_cmp_gt_i32_e64 s[52:53], v10, v113
	v_or_b32_e32 v10, 0x52, v8
	v_cmp_gt_i32_e64 s[54:55], v7, v113
	v_or_b32_e32 v7, 0x61, v8
	v_cmp_gt_i32_e64 s[56:57], v10, v113
	v_or_b32_e32 v10, 0x60, v8
	v_cmp_gt_i32_e64 s[58:59], v7, v113
	v_or_b32_e32 v7, 0x63, v8
	v_writelane_b32 v255, s30, 8
	v_cmp_gt_i32_e64 s[60:61], v10, v113
	v_or_b32_e32 v10, 0x62, v8
	v_cmp_gt_i32_e64 s[62:63], v7, v113
	v_or_b32_e32 v7, 0x71, v8
	s_cselect_b64 s[24:25], -1, 0
	v_writelane_b32 v255, s31, 9
	v_cmp_gt_i32_e64 s[64:65], v10, v113
	v_or_b32_e32 v10, 0x70, v8
	v_cmp_gt_i32_e64 s[66:67], v7, v113
	v_or_b32_e32 v7, 0x73, v8
	s_lshl_b32 s28, s28, 6
	v_lshlrev_b32_e32 v107, 1, v2
	v_add_u32_e32 v11, 0, v115
	v_mul_u32_u24_e32 v5, 0x110, v5
	s_mov_b32 s33, s74
	v_cmp_gt_i32_e64 s[68:69], v10, v113
	v_or_b32_e32 v10, 0x72, v8
	v_cmp_gt_i32_e64 s[70:71], v7, v113
	v_mul_u32_u24_e32 v7, 0x440, v9
	v_writelane_b32 v255, s28, 10
	v_cmp_gt_i32_e64 s[6:7], 64, v2
	v_add_u32_e32 v120, v114, v119
	v_cmp_gt_i32_e64 s[72:73], v10, v113
	v_add_u32_e32 v139, 0xfffffe00, v2
	s_lshl_b32 s37, s74, 6
	v_add_u32_e32 v141, 0x80, v107
	v_add_u32_e32 v142, 0x80, v106
	v_lshlrev_b32_e32 v2, 1, v4
	v_lshlrev_b32_e32 v96, 1, v6
	v_lshlrev_b32_e32 v98, 1, v8
	v_add_u32_e32 v143, v14, v7
	v_add_u32_e32 v144, v15, v5
	v_add_u32_e32 v145, v16, v5
	v_add_u32_e32 v146, v11, v5
	v_add_u32_e32 v147, v12, v5
	v_add_u32_e32 v148, v13, v5
	v_writelane_b32 v255, s33, 11
	s_branch .LBB0_662

; __device__ __forceinline__ unsigned xb_ld(unsigned* p)              { return __hip_atomic_load(p, __ATOMIC_RELAXED, __HIP_MEMORY_SCOPE_AGENT); }
; __device__ __forceinline__ unsigned xb_add(unsigned* p, unsigned v) { return __hip_atomic_fetch_add(p, v, __ATOMIC_RELAXED, __HIP_MEMORY_SCOPE_AGENT); }
; #define XB_SPIN(cond, bar) do { unsigned _sp = 0; while (cond) { __builtin_amdgcn_s_sleep(1); \
;     if ((++_sp & 255u) == 0u) { if (xb_ld(&(bar)[XB_TMO])) break; if (_sp > XB_SPIN_CAP) { atomicAdd(&(bar)[XB_TMO], 1u); break; } } } } while (0)
; __device__ __forceinline__ void xcd_barrier(const XcdBarrier& b) {
;     asm volatile("s_waitcnt vmcnt(0)" ::: "memory");
;     __syncthreads();
;     if (threadIdx.x == 0) {
;         unsigned* bar = b.bar;
;         __builtin_amdgcn_s_waitcnt(0);
;         unsigned nloc = b.st[0], nx = b.st[1];
;         if (nloc == 0u) { xcd_barrier_complete(bar, b.x, nloc, nx); b.st[0] = nloc; b.st[1] = nx; }
;         const unsigned old = xb_add(&bar[XB_XSUB(b.x)], 1u);
;         const unsigned gen = old / nloc;
;         if (old + 1u == (gen + 1u) * nloc) {
;             __builtin_amdgcn_fence(__ATOMIC_RELEASE, "agent");
;             asm volatile("s_waitcnt vmcnt(0)" ::: "memory");
;             const unsigned og = xb_add(&bar[XB_TOP], 1u);
;             const unsigned tg = og / nx;
;             if (og + 1u == (tg + 1u) * nx) xb_add(&bar[XB_TOPGEN], 1u);
;             else XB_SPIN(xb_ld(&bar[XB_TOPGEN]) == tg, bar);
;             __builtin_amdgcn_fence(__ATOMIC_ACQUIRE, "agent");
;             xb_add(&bar[XB_XGEN(b.x)], 1u);
;             asm volatile("s_waitcnt vmcnt(0)" ::: "memory");
;         } else {
;             XB_SPIN(xb_ld(&bar[XB_XGEN(b.x)]) == gen, bar);
;             __builtin_amdgcn_fence(__ATOMIC_ACQUIRE, "agent");
;             asm volatile("s_waitcnt vmcnt(0)" ::: "memory");
;         }
;     }
;     __syncthreads();
.LBB0_999:
	s_waitcnt vmcnt(0)
	s_barrier
	s_mov_b64 s[2:3], exec
	v_readlane_b32 s4, v253, 7
	v_readlane_b32 s5, v253, 8
	s_and_b64 s[4:5], s[2:3], s[4:5]
	s_mov_b32 s65, 0x800000
	s_mov_b64 exec, s[4:5]
	s_cbranch_execz .LBB0_1051
	s_mov_b32 s100, 3
	s_branch .Lxb_common
.Lxb_common:
	v_readlane_b32 s10, v253, 50
	v_mov_b32_e32 v2, 1
	s_nop 1
	v_mov_b32_e32 v1, s10
	ds_read_b32 v4, v1
	v_readlane_b32 s10, v253, 51
	s_nop 3
	v_mov_b32_e32 v1, s10
	ds_read_b32 v5, v1
	v_readlane_b32 s10, v253, 15
	v_readlane_b32 s11, v253, 16
	s_nop 4
	global_atomic_add v6, v3, v2, s[10:11] sc0
	s_waitcnt vmcnt(0) lgkmcnt(0)
	v_readfirstlane_b32 s12, v6
	v_readfirstlane_b32 s13, v4
	s_add_i32 vcc_lo, s101, 1
	s_mul_i32 s13, s13, vcc_lo
	s_add_i32 s12, s12, 1
	s_cmp_lg_u32 s12, s13
	s_cbranch_scc1 .Lxb_wait
	buffer_wbl2 sc1
	s_waitcnt vmcnt(0)
	v_readlane_b32 s10, v253, 19
	v_readlane_b32 s11, v253, 20
	s_nop 4
	global_atomic_add v6, v3, v2, s[10:11] sc0
	s_waitcnt vmcnt(0)
	v_readfirstlane_b32 s12, v6
	v_readfirstlane_b32 s13, v5
	s_mul_i32 s13, s13, vcc_lo
	s_add_i32 s12, s12, 1
	s_cmp_lg_u32 s12, s13
	s_cbranch_scc1 .Lxb_wait
	v_readlane_b32 s10, v253, 21
	v_readlane_b32 s11, v253, 22
	s_nop 4
	global_atomic_add v3, v2, s[10:11]
	v_readlane_b32 s10, v253, 63
	v_readlane_b32 s11, v254, 0
	s_nop 1
	s_add_u32 s10, s10, 0x2400
	s_addc_u32 s11, s11, 0
	s_nop 4
	global_atomic_add v3, v2, s[10:11]
	global_atomic_add v3, v2, s[10:11] offset:256
	global_atomic_add v3, v2, s[10:11] offset:512
	global_atomic_add v3, v2, s[10:11] offset:768
	global_atomic_add v3, v2, s[10:11] offset:1024
	global_atomic_add v3, v2, s[10:11] offset:1280
	global_atomic_add v3, v2, s[10:11] offset:1536
	global_atomic_add v3, v2, s[10:11] offset:1792
	global_atomic_add v3, v2, s[10:11] offset:2048
	global_atomic_add v3, v2, s[10:11] offset:2304
	global_atomic_add v3, v2, s[10:11] offset:2560
	global_atomic_add v3, v2, s[10:11] offset:2816
	global_atomic_add v3, v2, s[10:11] offset:3072
	global_atomic_add v3, v2, s[10:11] offset:3328
	global_atomic_add v3, v2, s[10:11] offset:3584
	global_atomic_add v3, v2, s[10:11] offset:3840
.Lxb_wait:
	v_readlane_b32 s10, v253, 17
	v_readlane_b32 s11, v253, 18
	s_mov_b32 s13, 0
	s_nop 4
.Lxb_spin:
	global_load_dword v6, v3, s[10:11] sc1
	s_waitcnt vmcnt(0)
	v_readfirstlane_b32 s12, v6
	s_cmp_lg_u32 s12, s101
	s_cbranch_scc1 .Lxb_released
	s_sleep 1
	s_add_i32 s13, s13, 1
	s_cmp_lt_u32 s13, 0x10000
	s_cbranch_scc1 .Lxb_spin
.Lxb_released:
	s_waitcnt vmcnt(0)
	buffer_inv sc1
	s_waitcnt vmcnt(0)
	s_cmp_eq_u32 s100, 1
	s_cbranch_scc1 .Lxb_ret_1
	s_cmp_eq_u32 s100, 2
	s_cbranch_scc1 .Lxb_ret_2
	s_cmp_eq_u32 s100, 3
	s_cbranch_scc1 .Lxb_ret_3
	s_cmp_eq_u32 s100, 4
	s_cbranch_scc1 .Lxb_ret_4
	s_cmp_eq_u32 s100, 5
	s_cbranch_scc1 .Lxb_ret_5
	s_cmp_eq_u32 s100, 6
	s_cbranch_scc1 .Lxb_ret_6
	s_cmp_eq_u32 s100, 8
	s_cbranch_scc1 .Lxb_ret_8
	s_cmp_eq_u32 s100, 9
	s_cbranch_scc1 .Lxb_ret_9
	s_branch .Lxb_ret_1
.Lxb_ret_3:
.LBB0_1051:
	s_or_b64 exec, exec, s[2:3]
	s_add_i32 s101, s101, 1
	s_mov_b32 s4, s93
	s_waitcnt vmcnt(1)
	v_mov_b32_e32 v36, v0
	v_readlane_b32 s2, v253, 3
	s_waitcnt lgkmcnt(0)
	s_barrier
	s_add_i32 s2, s4, s2
	v_readfirstlane_b32 s3, v36
	s_ashr_i32 s3, s3, 6
	s_lshl_b32 s2, s2, 3
	s_add_i32 s6, s3, s2
	s_cmpk_gt_i32 s6, 0x3fff
	s_mov_b64 s[2:3], -1
	s_cbranch_scc0 .LBB0_1053
	s_mov_b64 s[2:3], 0

;     __device__ void init2(int Mrows, int N, int G_, int c_, int reps_) { init(Mrows, N, G_, c_); per = (nwg + G - 1) / G; reps = reps_; }
; __device__ __forceinline__ unsigned xb_ld(unsigned* p)              { return __hip_atomic_load(p, __ATOMIC_RELAXED, __HIP_MEMORY_SCOPE_AGENT); }
; __device__ __forceinline__ unsigned xb_add(unsigned* p, unsigned v) { return __hip_atomic_fetch_add(p, v, __ATOMIC_RELAXED, __HIP_MEMORY_SCOPE_AGENT); }
; #define TS_BEGIN(k) do { if (TS_ON(k)) ts_t0 = __builtin_amdgcn_s_memrealtime(); } while (0)
; __device__ __forceinline__ void xcd_barrier(const XcdBarrier& b) {
;     asm volatile("s_waitcnt vmcnt(0)" ::: "memory");
;     __syncthreads();
;     if (threadIdx.x == 0) {
;         unsigned* bar = b.bar;
;         __builtin_amdgcn_s_waitcnt(0);
;         unsigned nloc = b.st[0], nx = b.st[1];
;         if (nloc == 0u) { xcd_barrier_complete(bar, b.x, nloc, nx); b.st[0] = nloc; b.st[1] = nx; }
;         const unsigned old = xb_add(&bar[XB_XSUB(b.x)], 1u);
;         const unsigned gen = old / nloc;
;         if (old + 1u == (gen + 1u) * nloc) {
;             __builtin_amdgcn_fence(__ATOMIC_RELEASE, "agent");
;             asm volatile("s_waitcnt vmcnt(0)" ::: "memory");
;             const unsigned og = xb_add(&bar[XB_TOP], 1u);
;             const unsigned tg = og / nx;
;             if (og + 1u == (tg + 1u) * nx) xb_add(&bar[XB_TOPGEN], 1u);
;             else XB_SPIN(xb_ld(&bar[XB_TOPGEN]) == tg, bar);
;             __builtin_amdgcn_fence(__ATOMIC_ACQUIRE, "agent");
;             xb_add(&bar[XB_XGEN(b.x)], 1u);
;             asm volatile("s_waitcnt vmcnt(0)" ::: "memory");
;         } else {
;             XB_SPIN(xb_ld(&bar[XB_XGEN(b.x)]) == gen, bar);
;             __builtin_amdgcn_fence(__ATOMIC_ACQUIRE, "agent");
;             asm volatile("s_waitcnt vmcnt(0)" ::: "memory");
;         }
;     }
;     __syncthreads();
; __global__ void __launch_bounds__(NWAVES * 64, 2) fwd(Params P) {
;     ...
;         if (IN(pb + 5)) {
;             PH_BEGIN
;             TS_BEGIN(5);
;             pg8::Gemm g{ymixb, Wout_t, D}; pg8::StaticOrder S; S.init(M, D, G, bx);
;             pg8::EpiBf16 E{(bf16_t*)mixed, FLD};
;     ...
;             { pg8::RepeatOrder R; R.init2(M, D, G, bx, 2); pg8::gemm_phase<pg8::EpiBf16, pg8::RepeatOrder>(lds, g, R, E, tid); }
;     ...
;             pg8::gemm_phase<pg8::EpiBf16, pg8::StaticOrder>(lds, g, S, E, tid);
.LBB0_1059:
	s_waitcnt vmcnt(0)
	s_barrier
	s_mov_b64 s[2:3], exec
	v_readlane_b32 s4, v253, 7
	v_readlane_b32 s5, v253, 8
	s_and_b64 s[4:5], s[2:3], s[4:5]
	s_mov_b64 exec, s[4:5]
	s_cbranch_execz .LBB0_1111
	s_mov_b32 s100, 4
	s_branch .Lxb_common
.Lxb_ret_4:
.LBB0_1111:
	s_or_b64 exec, exec, s[2:3]
	s_add_i32 s101, s101, 1
	s_mov_b32 s6, s93
	s_waitcnt lgkmcnt(0)
	s_barrier
	v_mov_b32_e32 v147, v0
	s_add_i32 s30, s6, s69
	s_cmpk_gt_i32 s30, 0x1ff
	v_readfirstlane_b32 s5, v147
	s_cbranch_scc1 .LBB0_1135
	s_ashr_i32 s31, s30, 31
	s_lshr_b32 s2, s31, 29
	s_add_i32 s8, s30, s2
	s_and_b32 s2, s8, -8
	s_sub_i32 s7, s30, s2
	s_cmp_gt_i32 s7, -1
	s_mov_b64 s[2:3], -1
	s_cbranch_scc0 .LBB0_1114
	s_lshl_b32 s4, s7, 6
	s_mov_b64 s[2:3], 0

; #define LAS __attribute__((address_space(3)))
; __device__ __forceinline__ unsigned xb_ld(unsigned* p)              { return __hip_atomic_load(p, __ATOMIC_RELAXED, __HIP_MEMORY_SCOPE_AGENT); }
; __device__ __forceinline__ void xcd_barrier(const XcdBarrier& b) {
;     asm volatile("s_waitcnt vmcnt(0)" ::: "memory");
;     __syncthreads();
;     if (threadIdx.x == 0) {
;         unsigned* bar = b.bar;
;         __builtin_amdgcn_s_waitcnt(0);
;         unsigned nloc = b.st[0], nx = b.st[1];
;         if (nloc == 0u) { xcd_barrier_complete(bar, b.x, nloc, nx); b.st[0] = nloc; b.st[1] = nx; }
;         const unsigned old = xb_add(&bar[XB_XSUB(b.x)], 1u);
;         const unsigned gen = old / nloc;
;         if (old + 1u == (gen + 1u) * nloc) {
;             __builtin_amdgcn_fence(__ATOMIC_RELEASE, "agent");
;             asm volatile("s_waitcnt vmcnt(0)" ::: "memory");
;             const unsigned og = xb_add(&bar[XB_TOP], 1u);
;             const unsigned tg = og / nx;
;             if (og + 1u == (tg + 1u) * nx) xb_add(&bar[XB_TOPGEN], 1u);
;             else XB_SPIN(xb_ld(&bar[XB_TOPGEN]) == tg, bar);
;             __builtin_amdgcn_fence(__ATOMIC_ACQUIRE, "agent");
;             xb_add(&bar[XB_XGEN(b.x)], 1u);
;             asm volatile("s_waitcnt vmcnt(0)" ::: "memory");
;         } else {
;             XB_SPIN(xb_ld(&bar[XB_XGEN(b.x)]) == gen, bar);
;             __builtin_amdgcn_fence(__ATOMIC_ACQUIRE, "agent");
;             asm volatile("s_waitcnt vmcnt(0)" ::: "memory");
;         }
;     }
;     __syncthreads();
; __global__ void __launch_bounds__(NWAVES * 64, 2) fwd(Params P) {
;     ...
;         if (IN(pb + 6)) {
;             PH_BEGIN
;             TS_BEGIN(6);
;             const float* xin = INP(0);
;             f32x4 g8[8], b8[8];
; #pragma unroll
;             for (int j = 0; j < 8; ++j) { g8[j] = *(const f32x4*)(INP(24) + l * D + 4 * lane + 256 * j); b8[j] = *(const f32x4*)(INP(25) + l * D + 4 * lane + 256 * j); }
;             LAS float* rs = (LAS float*)lds;
;             LAS int* wgcnt = (LAS int*)(lds + 65536); LAS int* wgbase = wgcnt + 8; LAS int* rec = wgcnt + 16;
;             if (moe) { const float* router = INP(31) + (size_t)li * D * NE;
;                 for (int i = tid; i < D * NE; i += 512) rs[(i & 7) * D + (i >> 3)] = router[i];
;                 if (tid < 16) wgcnt[tid] = 0;
;                 __syncthreads(); }
.LBB0_1135:
	s_waitcnt vmcnt(0)
	s_waitcnt vmcnt(0)
	s_barrier
	s_mov_b64 s[2:3], exec
	v_readlane_b32 s4, v253, 7
	v_readlane_b32 s5, v253, 8
	s_and_b64 s[4:5], s[2:3], s[4:5]
	s_mov_b64 exec, s[4:5]
	s_cbranch_execz .LBB0_1187
	s_mov_b32 s100, 5
	s_branch .Lxb_common
.Lxb_ret_5:
.LBB0_1187:
	s_or_b64 exec, exec, s[2:3]
	s_add_i32 s101, s101, 1
	s_mov_b32 s16, s93
	s_waitcnt lgkmcnt(0)
	s_barrier
	s_ashr_i32 s17, s16, 31
	s_lshl_b64 s[2:3], s[16:17], 3
	v_readlane_b32 s4, v254, 3
	v_readlane_b32 s5, v254, 4
	s_add_u32 s6, s4, s2
	v_mov_b32_e32 v132, v0
	s_addc_u32 s7, s5, s3
	s_load_dwordx4 s[8:11], s[6:7], 0xc0
	s_lshl_b32 s92, s14, 11
	s_lshl_b64 s[18:19], s[92:93], 2
	v_and_b32_e32 v74, 63, v132
	v_lshlrev_b32_e32 v68, 4, v74
	s_waitcnt lgkmcnt(0)
	s_add_u32 s2, s8, s18
	s_addc_u32 s3, s9, s19
	v_mov_b32_e32 v69, v3
	s_add_u32 s4, s10, s18
	v_lshl_add_u64 v[36:37], s[2:3], 0, v[68:69]
	s_addc_u32 s5, s11, s19
	global_load_dwordx4 v[4:7], v68, s[2:3]
	global_load_dwordx4 v[8:11], v68, s[2:3] offset:1024
	global_load_dwordx4 v[12:15], v68, s[4:5]
	global_load_dwordx4 v[16:19], v68, s[4:5] offset:1024
	global_load_dwordx4 v[20:23], v68, s[2:3] offset:2048
	global_load_dwordx4 v[24:27], v68, s[2:3] offset:3072
	global_load_dwordx4 v[28:31], v68, s[4:5] offset:2048
	global_load_dwordx4 v[32:35], v68, s[4:5] offset:3072
	s_movk_i32 s2, 0x1000
	v_add_co_u32_e32 v56, vcc, s2, v36
	v_lshl_add_u64 v[38:39], s[4:5], 0, v[68:69]
	s_nop 0
	v_addc_co_u32_e32 v57, vcc, 0, v37, vcc
	v_add_co_u32_e32 v64, vcc, 0x1000, v38
	v_readlane_b32 s2, v254, 13
	s_nop 0
	v_addc_co_u32_e32 v65, vcc, 0, v39, vcc
	global_load_dwordx4 v[36:39], v[56:57], off
	global_load_dwordx4 v[40:43], v[56:57], off offset:1024
	global_load_dwordx4 v[44:47], v[64:65], off
	global_load_dwordx4 v[48:51], v[64:65], off offset:1024
	global_load_dwordx4 v[52:55], v[56:57], off offset:2048
	s_nop 0
	global_load_dwordx4 v[56:59], v[56:57], off offset:3072
	s_nop 0
	global_load_dwordx4 v[60:63], v[64:65], off offset:2048
	s_nop 0
	global_load_dwordx4 v[64:67], v[64:65], off offset:3072
	s_load_dwordx2 s[20:21], s[6:7], 0x0
	v_readlane_b32 s3, v254, 14
	s_andn2_b64 vcc, exec, s[2:3]
	v_readfirstlane_b32 s22, v132
	v_cndmask_b32_e64 v1, 0, 1, s[2:3]
	v_cmp_ne_u32_e64 s[4:5], 1, v1
	s_cbranch_vccnz .LBB0_1204
	s_movk_i32 s2, 0x4000
	v_cmp_gt_i32_e32 vcc, s2, v132
	s_and_saveexec_b64 s[2:3], vcc
	s_cbranch_execz .LBB0_1201
	s_load_dwordx2 s[6:7], s[6:7], 0xf8
	v_max_i32_e32 v1, 0x3e00, v132
	v_sub_u32_e32 v1, v1, v132
	v_add_u32_e32 v1, 0x1ff, v1
	s_movk_i32 s8, 0x1ff
	v_cmp_lt_u32_e32 vcc, s8, v1
	s_mov_b64 s[10:11], -1
	v_mov_b32_e32 v70, v132
	s_and_saveexec_b64 s[8:9], vcc
	s_cbranch_execz .LBB0_1198
	v_readlane_b32 s10, v254, 17
	v_lshrrev_b32_e32 v1, 9, v1
	s_lshl_b32 s92, s10, 14
	s_lshl_b64 s[10:11], s[92:93], 2
	v_add_u32_e32 v69, -1, v1
	s_waitcnt lgkmcnt(0)
	s_add_u32 s10, s6, s10
	v_add_u32_e32 v133, 0x200, v132
	v_lshrrev_b32_e32 v2, 1, v69
	s_addc_u32 s11, s7, s11
	v_add_u32_e32 v2, 1, v2
	v_cmp_lt_u32_e32 vcc, 5, v69
	v_mov_b64_e32 v[70:71], v[132:133]
	s_and_saveexec_b64 s[12:13], vcc
	s_cbranch_execz .LBB0_1194
	v_and_b32_e32 v69, -4, v2
	s_mov_b64 s[14:15], 0
	v_mov_b64_e32 v[70:71], v[132:133]

; template <class Epi, class Sched, bool GATHER = false>
; __device__ __forceinline__ void gemm_phase(LAS unsigned char* lds, const Gemm g, const Sched& S, const Epi& E, const int tid) {
;     const int wid = __builtin_amdgcn_readfirstlane(tid >> 6), lane = tid & 63, wr = wid >> 2, wc = wid & 3, fr = lane & 15, fq = lane >> 4;
;     const int K = g.K, nt = K / BK;
;     unsigned voffA[2], voffB[2];
; #pragma unroll
;     for (int i = 0; i < 2; ++i) { int R, C; stage_rc(tid * 16 + i * 8192, R, C); const int Rb = Epi::PERM ? ((R & ~31) + perm32(R & 31)) : R;
;         voffA[i] = (unsigned)(R * K + C) * 2u; voffB[i] = (unsigned)(Rb * K + C) * 2u; }
;     unsigned goC[2][2], goN[2][2];
;     ...
;     const size_t kstep = (size_t)(BK * 2);
;     const size_t hstep = (size_t)HALF * K * 2;
;     const size_t tstep = 2 * hstep;
;     const unsigned ldsw = (unsigned)wid * 1024u;
;     const int aoff = lds_byte(wr * 64 + fr, fq * 8), boff = lds_byte(wc * 32 + fr, fq * 8);
;     ...
;     Unit cur, nxt; int ui = 0;
;     if (!S.next(0, cur)) return;
; __device__ __forceinline__ void xcd_barrier(const XcdBarrier& b) {
;     asm volatile("s_waitcnt vmcnt(0)" ::: "memory");
;     __syncthreads();
;     if (threadIdx.x == 0) {
;         unsigned* bar = b.bar;
;         __builtin_amdgcn_s_waitcnt(0);
;         unsigned nloc = b.st[0], nx = b.st[1];
;         if (nloc == 0u) { xcd_barrier_complete(bar, b.x, nloc, nx); b.st[0] = nloc; b.st[1] = nx; }
;         const unsigned old = xb_add(&bar[XB_XSUB(b.x)], 1u);
;         const unsigned gen = old / nloc;
;         if (old + 1u == (gen + 1u) * nloc) {
;             __builtin_amdgcn_fence(__ATOMIC_RELEASE, "agent");
;             asm volatile("s_waitcnt vmcnt(0)" ::: "memory");
;             const unsigned og = xb_add(&bar[XB_TOP], 1u);
;             const unsigned tg = og / nx;
;             if (og + 1u == (tg + 1u) * nx) xb_add(&bar[XB_TOPGEN], 1u);
;             else XB_SPIN(xb_ld(&bar[XB_TOPGEN]) == tg, bar);
;             __builtin_amdgcn_fence(__ATOMIC_ACQUIRE, "agent");
;             xb_add(&bar[XB_XGEN(b.x)], 1u);
;             asm volatile("s_waitcnt vmcnt(0)" ::: "memory");
;         } else {
;             XB_SPIN(xb_ld(&bar[XB_XGEN(b.x)]) == gen, bar);
;             __builtin_amdgcn_fence(__ATOMIC_ACQUIRE, "agent");
;             asm volatile("s_waitcnt vmcnt(0)" ::: "memory");
;         }
;     }
;     __syncthreads();
; }
.LBB0_1305:
	s_waitcnt lgkmcnt(0)
	s_barrier
	s_waitcnt vmcnt(0)
	s_barrier
	s_mov_b64 s[2:3], exec
	v_readlane_b32 s6, v253, 7
	v_readlane_b32 s7, v253, 8
	s_and_b64 s[6:7], s[2:3], s[6:7]
	s_mov_b64 exec, s[6:7]
	s_cbranch_execz .LBB0_1357
	s_mov_b32 s100, 6
	s_branch .Lxb_common
.Lxb_ret_6:
.LBB0_1357:
	s_or_b64 exec, exec, s[2:3]
	s_add_i32 s101, s101, 1
	s_mov_b32 s46, s93
	s_waitcnt lgkmcnt(0)
	s_barrier
	s_ashr_i32 s47, s46, 31
	v_readlane_b32 s2, v253, 4
	v_readlane_b32 s3, v253, 5
	s_add_u32 s48, s2, s46
	v_readlane_b32 s2, v253, 2
	s_addc_u32 s49, s3, s47
	s_add_i32 s44, s46, s2
	s_add_i32 s45, s46, s69
	s_add_u32 s12, s48, 0xa200000
	v_readlane_b32 s2, v254, 11
	s_addc_u32 s13, s49, 0
	v_readlane_b32 s3, v254, 12
	s_add_u32 s14, s48, 0x4c000000
	v_mov_b32_e32 v134, v0
	v_cndmask_b32_e64 v1, 0, 1, s[2:3]
	s_addc_u32 s15, s49, 0
	v_cmp_ne_u32_e64 s[6:7], 1, v1
	s_andn2_b64 vcc, exec, s[2:3]
	s_mov_b64 s[2:3], -1
	s_cbranch_vccnz .LBB0_1375
	s_cmpk_gt_i32 s45, 0xaff
	v_readfirstlane_b32 s9, v134
	s_cbranch_scc1 .LBB0_1374
	v_lshlrev_b32_e32 v1, 4, v134
	s_waitcnt vmcnt(15)
	v_add_u32_e32 v4, 0x2000, v1
	v_ashrrev_i32_e32 v2, 31, v4
	v_lshrrev_b32_e32 v2, 22, v2
	v_add_u32_e32 v2, v4, v2
	v_ashrrev_i32_e32 v2, 10, v2
	v_mul_i32_i24_e32 v5, 0x400, v2
	v_sub_u32_e32 v4, v4, v5
	v_lshrrev_b32_e32 v5, 4, v4
	v_bitop3_b32 v4, v5, v4, 32 bitop3:0x6c
	v_ashrrev_i32_e32 v5, 31, v4
	v_lshrrev_b32_e32 v5, 26, v5
	v_add_u32_e32 v5, v4, v5
	v_lshlrev_b32_e32 v6, 3, v2
	v_ashrrev_i32_e32 v146, 6, v5
	v_and_b32_e32 v6, -16, v6
	v_add_u32_e32 v6, v146, v6
	v_and_b32_e32 v7, 3, v146
	s_mov_b32 s2, 0xfffe0
	s_waitcnt vmcnt(14)
	v_lshrrev_b32_e32 v8, 2, v6
	v_lshlrev_b32_e32 v9, 1, v6
	v_and_b32_e32 v5, 0xc0, v5
	v_and_or_b32 v7, v6, s2, v7
	v_and_b32_e32 v8, 4, v8
	v_and_b32_e32 v9, 24, v9
	v_sub_u32_e32 v4, v4, v5
	v_or3_b32 v7, v7, v8, v9
	v_lshlrev_b32_e32 v8, 5, v2
	v_ashrrev_i16_sdwa v4, v236, sext(v4) dst_sel:DWORD dst_unused:UNUSED_PAD src0_sel:DWORD src1_sel:BYTE_0
	v_and_b32_e32 v8, 32, v8
	v_bfe_i32 v147, v4, 0, 16
	v_add_lshl_u32 v4, v8, v147, 1
	v_lshl_add_u32 v136, v7, 12, v4
	v_lshl_add_u32 v138, v6, 12, v4
	v_bfe_i32 v4, v134, 27, 1
	v_lshrrev_b32_e32 v4, 22, v4
	v_add_u32_e32 v4, v1, v4
	v_and_b32_e32 v4, 0xfffffc00, v4
	v_sub_u32_e32 v1, v1, v4
	v_lshrrev_b32_e32 v4, 4, v1
	v_ashrrev_i32_e32 v5, 31, v134
	v_bitop3_b32 v1, v4, v1, 32 bitop3:0x6c
	v_lshrrev_b32_e32 v5, 26, v5
	v_ashrrev_i32_e32 v4, 31, v1
	v_add_u32_e32 v5, v134, v5
	v_lshrrev_b32_e32 v4, 26, v4
	v_ashrrev_i32_e32 v145, 6, v5
	v_add_u32_e32 v4, v1, v4
	v_lshlrev_b32_e32 v5, 3, v145
	v_ashrrev_i32_e32 v144, 6, v4
	v_and_b32_e32 v5, -16, v5
	v_add_u32_e32 v5, v144, v5
	v_and_b32_e32 v6, 3, v144
	s_ashr_i32 s51, s45, 31
	v_and_or_b32 v6, v5, s2, v6
	s_lshr_b32 s2, s51, 29
	s_add_i32 s2, s45, s2
	s_ashr_i32 s17, s9, 6
	s_and_b32 s3, s2, -8
	s_ashr_i32 s16, s9, 8
	s_lshl_b32 s50, s17, 10
	s_sub_i32 s3, s45, s3
	s_cmp_lt_i32 s3, 0
	s_movk_i32 s8, 0x161
	s_cselect_b32 s8, s8, 0x160
	s_mul_i32 s3, s3, s8
	s_ashr_i32 s2, s2, 3
	s_add_i32 s3, s3, s2
	s_mul_hi_i32 s2, s3, 0x2e8ba2e9
	s_lshr_b32 s8, s2, 31
	s_ashr_i32 s2, s2, 6
	s_add_i32 s2, s2, s8
	s_lshl_b32 s10, s2, 3
	s_mulk_i32 s2, 0x160
	s_sub_i32 s2, s3, s2
	s_bfe_u32 s3, s2, 0x3001c
	s_add_i32 s3, s2, s3
	s_sext_i32_i16 s8, s3
	s_and_b32 s3, s3, 0xfff8
	s_sub_i32 s2, s2, s3
	s_sext_i32_i16 s2, s2
	v_lshrrev_b32_e32 v7, 2, v5
	v_lshlrev_b32_e32 v8, 1, v5
	v_and_b32_e32 v4, 0xc0, v4
	s_lshr_b32 s8, s8, 3
	s_add_i32 s30, s10, s2
	v_and_b32_e32 v7, 4, v7
	v_and_b32_e32 v8, 24, v8
	v_sub_u32_e32 v1, v1, v4
	s_ashr_i32 s31, s30, 31
	s_bfe_i64 s[10:11], s[8:9], 0x100000
	v_or3_b32 v6, v6, v7, v8
	v_lshlrev_b32_e32 v7, 5, v145
	v_ashrrev_i16_sdwa v1, v236, sext(v1) dst_sel:DWORD dst_unused:UNUSED_PAD src0_sel:DWORD src1_sel:BYTE_0
	s_lshl_b64 s[2:3], s[30:31], 20
	s_lshl_b64 s[10:11], s[10:11], 20
	v_and_b32_e32 v7, 32, v7
	v_bfe_i32 v148, v1, 0, 16
	s_add_u32 s36, s14, s10
	v_add_lshl_u32 v1, v7, v148, 1
	s_addc_u32 s37, s15, s11
	s_add_i32 s31, s50, 0
	v_lshl_add_u32 v140, v6, 12, v1
	v_lshl_add_u32 v142, v5, 12, v1
	s_waitcnt vmcnt(10)
	v_mov_b32_e32 v25, v3
	v_mov_b32_e32 v24, v3
	v_mov_b32_e32 v23, v3
	v_mov_b32_e32 v22, v3
	v_mov_b32_e32 v21, v3
	v_mov_b32_e32 v20, v3
	v_mov_b32_e32 v19, v3
	v_mov_b32_e32 v18, v3
	s_waitcnt vmcnt(9)
	v_mov_b32_e32 v28, v3
	v_mov_b32_e32 v27, v3
	v_mov_b32_e32 v26, v3
	v_mov_b32_e32 v17, v3
	v_mov_b32_e32 v16, v3
	v_mov_b32_e32 v15, v3
	v_mov_b32_e32 v14, v3
	v_mov_b32_e32 v13, v3
	v_mov_b32_e32 v12, v3
	v_mov_b32_e32 v11, v3
	v_mov_b32_e32 v10, v3
	v_mov_b32_e32 v7, v3
	v_mov_b32_e32 v6, v3
	s_waitcnt vmcnt(1)
	v_mov_b32_e32 v63, v3
	v_mov_b32_e32 v62, v3
	v_mov_b32_e32 v89, v3
	v_mov_b32_e32 v88, v3
	v_mov_b32_e32 v87, v3
	v_mov_b32_e32 v86, v3
	v_mov_b32_e32 v85, v3
	v_mov_b32_e32 v84, v3
	v_mov_b32_e32 v83, v3
	v_mov_b32_e32 v82, v3
	v_mov_b32_e32 v1, v3
	s_add_i32 m0, s31, 0x10000
	s_nop 0
	global_load_lds_dwordx4 v140, s[36:37]
	s_add_i32 m0, s31, 0x12000
	s_add_u32 s10, s36, 0x80000
	global_load_lds_dwordx4 v136, s[36:37]
	s_addc_u32 s11, s37, 0
	s_add_i32 m0, s31, 0x14000
	v_mov_b32_e32 v141, v3
	global_load_lds_dwordx4 v140, s[10:11]
	s_add_i32 m0, s31, 0x16000
	s_add_u32 s34, s12, s2
	s_addc_u32 s35, s13, s3
	s_add_i32 s52, s31, 0x2000
	global_load_lds_dwordx4 v136, s[10:11]
	s_mov_b32 m0, s31
	s_add_u32 s2, s34, 0x80000
	global_load_lds_dwordx4 v142, s[34:35]
	s_mov_b32 m0, s52
	s_addc_u32 s3, s35, 0
	s_add_i32 s53, s31, 0x4000
	global_load_lds_dwordx4 v138, s[34:35]
	s_mov_b32 m0, s53
	s_add_i32 s54, s31, 0x6000
	global_load_lds_dwordx4 v142, s[2:3]
	s_mov_b32 m0, s54
	v_mov_b32_e32 v137, v3
	global_load_lds_dwordx4 v138, s[2:3]
	v_mov_b32_e32 v143, v3
	v_mov_b32_e32 v139, v3
	s_cmp_eq_u32 s16, 1
	v_lshl_add_u64 v[56:57], s[36:37], 0, v[140:141]
	v_lshl_add_u64 v[54:55], s[36:37], 0, v[136:137]
	v_lshl_add_u64 v[4:5], s[34:35], 0, v[142:143]
	s_cselect_b64 s[2:3], -1, 0
	s_cmp_lg_u32 s16, 1
	v_lshl_add_u64 v[8:9], s[34:35], 0, v[138:139]
	s_cbranch_scc1 .LBB0_1361
	s_barrier

;     __device__ __forceinline__ bool next(int i, Unit& u) const { if (i >= per * reps) return false; return StaticOrder::next(i % per, u); }
; __device__ __forceinline__ unsigned xb_ld(unsigned* p)              { return __hip_atomic_load(p, __ATOMIC_RELAXED, __HIP_MEMORY_SCOPE_AGENT); }
; __device__ __forceinline__ unsigned xb_add(unsigned* p, unsigned v) { return __hip_atomic_fetch_add(p, v, __ATOMIC_RELAXED, __HIP_MEMORY_SCOPE_AGENT); }
; #define XB_SPIN(cond, bar) do { unsigned _sp = 0; while (cond) { __builtin_amdgcn_s_sleep(1); \
;     if ((++_sp & 255u) == 0u) { if (xb_ld(&(bar)[XB_TMO])) break; if (_sp > XB_SPIN_CAP) { atomicAdd(&(bar)[XB_TMO], 1u); break; } } } } while (0)
;     __device__ __forceinline__ bool next(int i, Unit& u) const {
;         const long L = (long)i * G + c; if (L >= nwg) return false;
;         decode_unit((int)L, nM, nN, u.pm, u.pn); u.pb = u.pn; return true;
; __device__ __forceinline__ void xcd_barrier(const XcdBarrier& b) {
;     asm volatile("s_waitcnt vmcnt(0)" ::: "memory");
;     __syncthreads();
;     if (threadIdx.x == 0) {
;         unsigned* bar = b.bar;
;         __builtin_amdgcn_s_waitcnt(0);
;         unsigned nloc = b.st[0], nx = b.st[1];
;         if (nloc == 0u) { xcd_barrier_complete(bar, b.x, nloc, nx); b.st[0] = nloc; b.st[1] = nx; }
;         const unsigned old = xb_add(&bar[XB_XSUB(b.x)], 1u);
;         const unsigned gen = old / nloc;
;         if (old + 1u == (gen + 1u) * nloc) {
;             __builtin_amdgcn_fence(__ATOMIC_RELEASE, "agent");
;             asm volatile("s_waitcnt vmcnt(0)" ::: "memory");
;             const unsigned og = xb_add(&bar[XB_TOP], 1u);
;             const unsigned tg = og / nx;
;             if (og + 1u == (tg + 1u) * nx) xb_add(&bar[XB_TOPGEN], 1u);
;             else XB_SPIN(xb_ld(&bar[XB_TOPGEN]) == tg, bar);
;             __builtin_amdgcn_fence(__ATOMIC_ACQUIRE, "agent");
;             xb_add(&bar[XB_XGEN(b.x)], 1u);
;             asm volatile("s_waitcnt vmcnt(0)" ::: "memory");
;         } else {
;             XB_SPIN(xb_ld(&bar[XB_XGEN(b.x)]) == gen, bar);
;             __builtin_amdgcn_fence(__ATOMIC_ACQUIRE, "agent");
;             asm volatile("s_waitcnt vmcnt(0)" ::: "memory");
;         }
;     }
;     __syncthreads();
; }
.LBB0_1409:
	s_waitcnt vmcnt(0)
	s_waitcnt vmcnt(0)
	s_barrier
	s_mov_b64 s[2:3], exec
	v_readlane_b32 s8, v253, 7
	v_readlane_b32 s9, v253, 8
	v_readlane_b32 s20, v253, 63
	v_readlane_b32 s22, v253, 9
	v_readlane_b32 s24, v253, 11
	v_readlane_b32 s28, v253, 13
	v_readlane_b32 s30, v253, 17
	s_and_b64 s[8:9], s[2:3], s[8:9]
	v_readlane_b32 s21, v254, 0
	v_readlane_b32 s23, v253, 10
	v_readlane_b32 s25, v253, 12
	v_readlane_b32 s29, v253, 14
	v_readlane_b32 s31, v253, 18
	s_movk_i32 s48, 0x5cc0
	s_movk_i32 s49, 0x800
	s_movk_i32 s50, 0xa0
	s_mov_b64 exec, s[8:9]
	s_cbranch_execz .LBB0_1461
	s_mov_b32 s100, 8
	s_branch .Lxb_common
.Lxb_ret_8:
.LBB0_1461:
	s_or_b64 exec, exec, s[2:3]
	s_add_i32 s101, s101, 1
	s_mov_b32 s22, s93
	s_waitcnt lgkmcnt(0)
	s_barrier
	s_ashr_i32 s23, s22, 31
	v_readlane_b32 s2, v253, 4
	v_readlane_b32 s3, v253, 5
	s_add_u32 s20, s2, s22
	v_readlane_b32 s2, v253, 2
	s_addc_u32 s21, s3, s23
	s_add_i32 s37, s22, s2
	s_add_i32 s36, s22, s69
	v_mov_b32_e32 v1, v0
	s_add_u32 s39, s20, 0x16400000
	s_addc_u32 s40, s21, 0
	v_readfirstlane_b32 s38, v1
	s_and_b64 vcc, exec, s[6:7]
	s_mov_b64 s[2:3], -1
	s_cbranch_vccnz .LBB0_1491
	s_cmpk_gt_i32 s36, 0x1ff
	v_readfirstlane_b32 s8, v1
	s_cbranch_scc1 .LBB0_1490
	s_ashr_i32 s41, s36, 31
	s_lshr_b32 s2, s41, 29
	s_add_i32 s11, s36, s2
	s_and_b32 s2, s11, -8
	s_sub_i32 s9, s36, s2
	s_cmp_gt_i32 s9, -1
	s_mov_b64 s[2:3], -1
	s_cbranch_scc0 .LBB0_1465
	s_lshl_b32 s12, s9, 6
	s_mov_b64 s[2:3], 0

; __device__ __forceinline__ unsigned xb_ld(unsigned* p)              { return __hip_atomic_load(p, __ATOMIC_RELAXED, __HIP_MEMORY_SCOPE_AGENT); }
; __device__ __forceinline__ unsigned xb_add(unsigned* p, unsigned v) { return __hip_atomic_fetch_add(p, v, __ATOMIC_RELAXED, __HIP_MEMORY_SCOPE_AGENT); }
; __device__ __forceinline__ void xcd_barrier(const XcdBarrier& b) {
;     asm volatile("s_waitcnt vmcnt(0)" ::: "memory");
;     __syncthreads();
;     if (threadIdx.x == 0) {
;         unsigned* bar = b.bar;
;         __builtin_amdgcn_s_waitcnt(0);
;         unsigned nloc = b.st[0], nx = b.st[1];
;         if (nloc == 0u) { xcd_barrier_complete(bar, b.x, nloc, nx); b.st[0] = nloc; b.st[1] = nx; }
;         const unsigned old = xb_add(&bar[XB_XSUB(b.x)], 1u);
;         const unsigned gen = old / nloc;
;         if (old + 1u == (gen + 1u) * nloc) {
;             __builtin_amdgcn_fence(__ATOMIC_RELEASE, "agent");
;             asm volatile("s_waitcnt vmcnt(0)" ::: "memory");
;             const unsigned og = xb_add(&bar[XB_TOP], 1u);
;             const unsigned tg = og / nx;
;             if (og + 1u == (tg + 1u) * nx) xb_add(&bar[XB_TOPGEN], 1u);
;             else XB_SPIN(xb_ld(&bar[XB_TOPGEN]) == tg, bar);
;             __builtin_amdgcn_fence(__ATOMIC_ACQUIRE, "agent");
;             xb_add(&bar[XB_XGEN(b.x)], 1u);
;             asm volatile("s_waitcnt vmcnt(0)" ::: "memory");
;         } else {
;             XB_SPIN(xb_ld(&bar[XB_XGEN(b.x)]) == gen, bar);
;             __builtin_amdgcn_fence(__ATOMIC_ACQUIRE, "agent");
;             asm volatile("s_waitcnt vmcnt(0)" ::: "memory");
;         }
;     }
;     __syncthreads();
; }
; __global__ void __launch_bounds__(NWAVES * 64, 2) fwd(Params P) {
;     ...
;             f32x4 g8[8], b8[8];
; #pragma unroll
;             for (int j = 0; j < 8; ++j) { g8[j] = *(const f32x4*)(INP(26) + l * D + 4 * lane + 256 * j); b8[j] = *(const f32x4*)(INP(27) + l * D + 4 * lane + 256 * j); }
;             float* dst = (l == 3) ? P.out : (float*)nullptr; const bf16_t* ysb = (const bf16_t*)yslot;
;             int pstart[8]; { int acc_ = 0;
; #pragma unroll
;                 for (int e = 0; e < 8; ++e) { pstart[e] = acc_; acc_ += moe ? (((cnt[e] + 255) >> 8) << 8) : 0; } }
.LBB0_1731:
	s_waitcnt vmcnt(0)
	s_waitcnt vmcnt(0) lgkmcnt(0)
	s_barrier
	s_mov_b64 s[8:9], exec
	v_readlane_b32 s10, v253, 7
	v_readlane_b32 s11, v253, 8
	s_and_b64 s[10:11], s[8:9], s[10:11]
	s_mov_b64 exec, s[10:11]
	s_cbranch_execz .LBB0_1783
	s_mov_b32 s100, 9
	s_branch .Lxb_common
.Lxb_ret_9:
.LBB0_1783:
	s_or_b64 exec, exec, s[8:9]
	s_add_i32 s101, s101, 1
	s_mov_b32 s8, s93
	s_waitcnt lgkmcnt(0)
	s_barrier
	s_ashr_i32 s9, s8, 31
	s_lshl_b64 s[10:11], s[8:9], 3
	s_add_u32 s10, s74, s10
	v_mov_b32_e32 v68, v0
	s_addc_u32 s11, s75, s11
	s_load_dwordx4 s[12:15], s[10:11], 0xd0
	v_lshlrev_b32_e32 v1, 2, v68
	v_and_b32_e32 v69, 0xfc, v1
	v_lshlrev_b32_e32 v76, 2, v69
	v_mov_b32_e32 v77, v3
	s_waitcnt lgkmcnt(0)
	s_add_u32 s10, s12, s18
	s_addc_u32 s11, s13, s19
	s_add_u32 s12, s14, s18
	v_lshl_add_u64 v[36:37], s[10:11], 0, v[76:77]
	s_addc_u32 s13, s15, s19
	global_load_dwordx4 v[4:7], v76, s[10:11]
	global_load_dwordx4 v[8:11], v76, s[10:11] offset:1024
	global_load_dwordx4 v[12:15], v76, s[12:13]
	global_load_dwordx4 v[16:19], v76, s[12:13] offset:1024
	global_load_dwordx4 v[20:23], v76, s[10:11] offset:2048
	global_load_dwordx4 v[24:27], v76, s[10:11] offset:3072
	global_load_dwordx4 v[28:31], v76, s[12:13] offset:2048
	global_load_dwordx4 v[32:35], v76, s[12:13] offset:3072
	s_movk_i32 s10, 0x1000
	v_add_co_u32_e32 v56, vcc, s10, v36
	v_lshl_add_u64 v[38:39], s[12:13], 0, v[76:77]
	s_nop 0
	v_addc_co_u32_e32 v57, vcc, 0, v37, vcc
	v_add_co_u32_e32 v64, vcc, s10, v38
	v_readlane_b32 s10, v253, 4
	s_nop 0
	v_addc_co_u32_e32 v65, vcc, 0, v39, vcc
	global_load_dwordx4 v[36:39], v[56:57], off
	global_load_dwordx4 v[40:43], v[56:57], off offset:1024
	global_load_dwordx4 v[44:47], v[64:65], off
	global_load_dwordx4 v[48:51], v[64:65], off offset:1024
	global_load_dwordx4 v[52:55], v[56:57], off offset:2048
	s_nop 0
	global_load_dwordx4 v[56:59], v[56:57], off offset:3072
	s_nop 0
	global_load_dwordx4 v[60:63], v[64:65], off offset:2048
	s_nop 0
	global_load_dwordx4 v[64:67], v[64:65], off offset:3072
	v_readlane_b32 s11, v253, 5
	s_add_u32 s20, s10, s8
	v_readlane_b32 s10, v254, 17
	s_addc_u32 s21, s11, s9
	s_lshl_b32 s92, s10, 3
	s_lshl_b64 s[10:11], s[92:93], 2
	v_readlane_b32 s14, v254, 13
	s_add_u32 s10, s20, s10
	v_readlane_b32 s15, v254, 14
	v_readfirstlane_b32 s12, v68
	s_addc_u32 s11, s21, s11
	s_and_b64 vcc, exec, s[14:15]
	v_mov_b32_e32 v1, 0
	s_cbranch_vccz .LBB0_1785
	global_load_dword v1, v3, s[10:11] offset:64
	s_waitcnt vmcnt(0)
	v_add_u32_e32 v1, 0xff, v1
	v_and_b32_e32 v1, 0xffffff00, v1

; __global__ void __launch_bounds__(NWAVES * 64, 2) fwd(Params P) {
;     extern __shared__ __attribute__((aligned(16))) unsigned char lds_raw[];
	.amdhsa_kernel _ZN12_GLOBAL__N_13fwdENS_6ParamsE
		.amdhsa_group_segment_fixed_size 0
		.amdhsa_private_segment_fixed_size 0
		.amdhsa_kernarg_size 568
		.amdhsa_user_sgpr_count 2
		.amdhsa_user_sgpr_dispatch_ptr 0
		.amdhsa_user_sgpr_queue_ptr 0
		.amdhsa_user_sgpr_kernarg_segment_ptr 1
		.amdhsa_user_sgpr_dispatch_id 0
		.amdhsa_user_sgpr_kernarg_preload_length 0
		.amdhsa_user_sgpr_kernarg_preload_offset 0
		.amdhsa_user_sgpr_private_segment_size 0
		.amdhsa_uses_dynamic_stack 0
		.amdhsa_enable_private_segment 0
		.amdhsa_system_sgpr_workgroup_id_x 1
		.amdhsa_system_sgpr_workgroup_id_y 0
		.amdhsa_system_sgpr_workgroup_id_z 0
		.amdhsa_system_sgpr_workgroup_info 0
		.amdhsa_system_vgpr_workitem_id 0
		.amdhsa_next_free_vgpr 256
		.amdhsa_next_free_sgpr 102
		.amdhsa_accum_offset 256
		.amdhsa_reserve_vcc 1
		.amdhsa_float_round_mode_32 0
		.amdhsa_float_round_mode_16_64 0
		.amdhsa_float_denorm_mode_32 3
		.amdhsa_float_denorm_mode_16_64 3
		.amdhsa_dx10_clamp 1
		.amdhsa_ieee_mode 1
		.amdhsa_fp16_overflow 0
		.amdhsa_tg_split 0
		.amdhsa_exception_fp_ieee_invalid_op 0
		.amdhsa_exception_fp_denorm_src 0
		.amdhsa_exception_fp_ieee_div_zero 0
		.amdhsa_exception_fp_ieee_overflow 0
		.amdhsa_exception_fp_ieee_underflow 0
		.amdhsa_exception_fp_ieee_inexact 0
		.amdhsa_exception_int_div_zero 0
	.end_amdhsa_kernel

amdhsa.kernels:
  - .agpr_count:     0
    .args:
      - .offset:         0
        .size:           312
        .value_kind:     by_value
      - .offset:         312
        .size:           4
        .value_kind:     hidden_block_count_x
      - .offset:         316
        .size:           4
        .value_kind:     hidden_block_count_y
      - .offset:         320
        .size:           4
        .value_kind:     hidden_block_count_z
      - .offset:         324
        .size:           2
        .value_kind:     hidden_group_size_x
      - .offset:         326
        .size:           2
        .value_kind:     hidden_group_size_y
      - .offset:         328
        .size:           2
        .value_kind:     hidden_group_size_z
      - .offset:         330
        .size:           2
        .value_kind:     hidden_remainder_x
      - .offset:         332
        .size:           2
        .value_kind:     hidden_remainder_y
      - .offset:         334
        .size:           2
        .value_kind:     hidden_remainder_z
      - .offset:         352
        .size:           8
        .value_kind:     hidden_global_offset_x
      - .offset:         360
        .size:           8
        .value_kind:     hidden_global_offset_y
      - .offset:         368
        .size:           8
        .value_kind:     hidden_global_offset_z
      - .offset:         376
        .size:           2
        .value_kind:     hidden_grid_dims
      - .offset:         432
        .size:           4
        .value_kind:     hidden_dynamic_lds_size
    .group_segment_fixed_size: 0
    .kernarg_segment_align: 8
    .kernarg_segment_size: 568
    .language:       OpenCL C
    .language_version:
      - 2
      - 0
    .max_flat_workgroup_size: 512
    .name:           _ZN12_GLOBAL__N_13fwdENS_6ParamsE
    .private_segment_fixed_size: 0
    .sgpr_count:     108
    .sgpr_spill_count: 181
    .symbol:         _ZN12_GLOBAL__N_13fwdENS_6ParamsE.kd
    .uniform_work_group_size: 1
    .uses_dynamic_stack: false
    .vgpr_count:     256
    .vgpr_spill_count: 0
    .wavefront_size: 64
